# dedicated conversion workgroups spread over all eight XCDs
# baseline (speedup 1.0000x reference)
.LBB0_454:
	s_cmp_gt_i32 s56, 3
	s_cselect_b64 s[0:1], -1, 0
	s_cmp_lt_i32 s57, 4
	s_cselect_b64 s[2:3], -1, 0
	s_or_b64 s[0:1], s[0:1], s[2:3]
	s_and_b64 vcc, exec, s[0:1]
	s_lshr_b32 s46, s87, 7
	s_sub_u32 s46, s87, s46
	s_mul_i32 s46, s46, 0xaaaaaaab
	s_cbranch_vccnz .LBB0_616
	s_add_i32 s1, s46, 0x2aaaaaaa
	s_mov_b32 s0, 0x2aaaaaaa
	v_alignbit_b32 v2, s1, s1, 1
	v_mov_b32_e32 v1, v0
	v_cmp_lt_u32_e32 vcc, s0, v2
	s_nop 0
	v_cmp_eq_u32_e64 s[0:1], 0, v1
	s_cbranch_vccnz .LBB0_472
	s_mul_i32 s2, s91, 0x4100
	s_add_i32 s2, s2, 0
	s_add_u32 s10, s92, 0xa000000
	s_waitcnt lgkmcnt(0)
	v_and_b32_e32 v3, 7, v1
	v_bfe_u32 v7, v1, 3, 3
	s_addc_u32 s11, s93, 0
	v_lshlrev_b32_e32 v2, 2, v7
	v_mul_u32_u24_e32 v4, 0x810, v3
	v_add3_u32 v8, s2, v2, v4
	v_lshl_add_u32 v4, v3, 6, s2
	s_waitcnt vmcnt(0)
	v_mul_u32_u24_e32 v13, 0x204, v7
	s_add_u32 s12, s92, 0x2000000
	v_mov_b32_e32 v5, 0
	s_addc_u32 s13, s93, 0
	s_add_i32 s15, 0, 0x27c00
	v_add_u32_e32 v13, v4, v13
	s_mov_b32 s3, 0
	v_lshlrev_b32_e32 v6, 2, v3
	v_lshlrev_b32_e32 v2, 4, v3
	v_mov_b32_e32 v3, v5
	v_or_b32_e32 v9, 8, v7
	v_or_b32_e32 v10, 16, v7
	v_or_b32_e32 v11, 24, v7
	s_movk_i32 s14, 0x3ff
	v_mov_b32_e32 v12, s15
	s_movk_i32 s16, 0xbff
	s_mov_b32 s17, 0x8000
	s_mov_b32 s18, 0x10000
	s_mov_b32 s19, 0x18000
	s_mov_b32 s20, 0x20000
	s_mov_b32 s21, 0x28000
	s_mov_b32 s22, 0x30000
	s_mov_b32 s23, 0x38000
	s_mov_b32 s24, 0x40000
	s_mov_b32 s25, 0x48000
	s_mov_b32 s26, 0x50000
	s_mov_b32 s27, 0x58000
	s_mov_b32 s28, 0x60000
	s_mov_b32 s29, 0x68000
	s_mov_b32 s30, 0x70000
	s_mov_b32 s31, 0x78000
	s_mov_b32 s33, 0xc3e00000
	v_add_u32_e32 v14, 0x1020, v13
	v_add_u32_e32 v15, 0x1028, v13
	v_add_u32_e32 v16, 0x1030, v13
	v_add_u32_e32 v17, 0x1038, v13
	v_add_u32_e32 v18, 0x1040, v13
	v_add_u32_e32 v19, 0x1048, v13
	v_add_u32_e32 v20, 0x1050, v13
	v_add_u32_e32 v21, 0x1058, v13
	v_add_u32_e32 v22, 0x2040, v13
	v_add_u32_e32 v23, 0x2048, v13
	v_add_u32_e32 v24, 0x2050, v13
	v_add_u32_e32 v25, 0x2058, v13
	v_add_u32_e32 v26, 0x2060, v13
	v_add_u32_e32 v27, 0x2068, v13
	v_add_u32_e32 v28, 0x2070, v13
	v_add_u32_e32 v29, 0x2078, v13
	v_add_u32_e32 v30, 0x3060, v13
	v_add_u32_e32 v31, 0x3068, v13
	v_add_u32_e32 v32, 0x3070, v13
	v_add_u32_e32 v33, 0x3078, v13
	v_add_u32_e32 v34, 0x3080, v13
	v_add_u32_e32 v35, 0x3088, v13
	v_add_u32_e32 v36, 0x3090, v13
	v_add_u32_e32 v37, 0x3098, v13
	s_mov_b32 s34, 0x80000
	s_mov_b32 s35, 0x90000
	s_mov_b32 s38, 0xa0000
	s_mov_b32 s39, 0xb0000
	s_mov_b32 s40, 0xc0000
	s_mov_b32 s41, 0xd0000
	s_mov_b32 s42, 0xe0000
	s_mov_b32 s43, 0xf0000
	v_add_u32_e32 v38, 0x400, v8
	v_mov_b32_e32 v39, 0x43e00000
	s_branch .LBB0_459
